# v39 with the P2 projection epilogue stores write-through (sc1: line dropped from L2) instead of nt
# speedup vs baseline: 1.0225x; 1.0225x over previous
.LBB0_215:
	v_mov_b32_e32 v130, v183
	v_cvt_pk_bf16_f32 v126, v126, v127
	v_cvt_pk_bf16_f32 v127, v128, v129
	v_cvt_pk_bf16_f32 v128, v122, v123
	v_cvt_pk_bf16_f32 v129, v124, v125
	v_cvt_pk_bf16_f32 v118, v118, v119
	s_nop 0
	v_and_b32_e32 v132, 7, v130
	v_lshlrev_b32_e32 v133, 7, v130
	v_lshrrev_b32_e32 v134, 3, v130
	v_and_b32_e32 v133, 0x780, v133
	v_bitop3_b32 v134, v134, v132, s57 bitop3:0x6c
	v_ashrrev_i32_e32 v131, 3, v130
	v_add_u32_e32 v133, s39, v133
	v_lshlrev_b32_e32 v134, 4, v134
	v_lshlrev_b32_e32 v135, 7, v131
	v_bitop3_b32 v130, v130, v131, 7 bitop3:0x6c
	v_add_u32_e32 v131, v133, v134
	v_lshlrev_b32_e32 v130, 4, v130
	ds_write_b128 v131, v[126:129]
	v_xad_u32 v126, v134, 16, v133
	v_add3_u32 v130, s39, v135, v130
	v_cvt_pk_bf16_f32 v119, v120, v121
	v_cvt_pk_bf16_f32 v120, v110, v111
	v_cvt_pk_bf16_f32 v121, v112, v113
	ds_write_b128 v126, v[118:121]
	ds_read_b128 v[118:121], v130
	ds_read_b128 v[122:125], v130 offset:1024
	v_lshl_or_b32 v112, v132, 4, s54
	v_mov_b32_e32 v113, v173
	v_lshl_add_u64 v[110:111], s[4:5], 0, v[112:113]
	s_waitcnt lgkmcnt(0)
	global_store_dwordx4 v112, v[118:121], s[4:5] sc1
	v_add_co_u32_e32 v112, vcc, s58, v110
	v_cvt_pk_bf16_f32 v102, v102, v103
	v_cvt_pk_bf16_f32 v103, v104, v105
	v_cvt_pk_bf16_f32 v104, v94, v95
	v_cvt_pk_bf16_f32 v105, v96, v97
	s_nop 1
	v_addc_co_u32_e32 v113, vcc, 0, v111, vcc
	global_store_dwordx4 v[112:113], v[122:125], off sc1
	v_cvt_pk_bf16_f32 v112, v114, v115
	v_cvt_pk_bf16_f32 v113, v116, v117
	v_cvt_pk_bf16_f32 v114, v106, v107
	v_cvt_pk_bf16_f32 v115, v108, v109
	ds_write_b128 v131, v[112:115]
	ds_write_b128 v126, v[102:105]
	ds_read_b128 v[94:97], v130
	ds_read_b128 v[102:105], v130 offset:1024
	v_add_co_u32_e32 v106, vcc, s59, v110
	v_cvt_pk_bf16_f32 v86, v86, v87
	v_cvt_pk_bf16_f32 v87, v88, v89
	v_cvt_pk_bf16_f32 v88, v78, v79
	v_cvt_pk_bf16_f32 v89, v80, v81
	s_nop 1
	v_addc_co_u32_e32 v107, vcc, 0, v111, vcc
	s_waitcnt lgkmcnt(0)
	global_store_dwordx4 v[106:107], v[94:97], off sc1
	v_cvt_pk_bf16_f32 v70, v70, v71
	v_cvt_pk_bf16_f32 v71, v72, v73
	v_cvt_pk_bf16_f32 v72, v66, v67
	v_cvt_pk_bf16_f32 v73, v68, v69
	v_cvt_pk_bf16_f32 v62, v62, v63
	s_nop 1
	v_add_co_u32_e32 v94, vcc, s60, v110
	v_cvt_pk_bf16_f32 v96, v90, v91
	v_cvt_pk_bf16_f32 v97, v92, v93
	v_cvt_pk_bf16_f32 v63, v64, v65
	v_cvt_pk_bf16_f32 v64, v58, v59
	s_nop 1
	v_addc_co_u32_e32 v95, vcc, 0, v111, vcc
	global_store_dwordx4 v[94:95], v[102:105], off sc1
	v_cvt_pk_bf16_f32 v94, v98, v99
	v_cvt_pk_bf16_f32 v95, v100, v101
	ds_write_b128 v131, v[94:97]
	ds_write_b128 v126, v[86:89]
	ds_read_b128 v[78:81], v130
	ds_read_b128 v[86:89], v130 offset:1024
	v_add_co_u32_e32 v90, vcc, s61, v110
	v_cvt_pk_bf16_f32 v65, v60, v61
	v_cvt_pk_bf16_f32 v54, v54, v55
	v_cvt_pk_bf16_f32 v55, v56, v57
	v_cvt_pk_bf16_f32 v56, v46, v47
	s_nop 1
	v_addc_co_u32_e32 v91, vcc, 0, v111, vcc
	s_waitcnt lgkmcnt(0)
	global_store_dwordx4 v[90:91], v[78:81], off sc1
	v_cvt_pk_bf16_f32 v57, v48, v49
	v_cvt_pk_bf16_f32 v38, v38, v39
	v_cvt_pk_bf16_f32 v39, v40, v41
	v_cvt_pk_bf16_f32 v40, v30, v31
	v_cvt_pk_bf16_f32 v41, v32, v33
	s_nop 1
	v_add_co_u32_e32 v78, vcc, s62, v110
	v_cvt_pk_bf16_f32 v80, v74, v75
	v_cvt_pk_bf16_f32 v81, v76, v77
	v_cvt_pk_bf16_f32 v22, v22, v23
	v_cvt_pk_bf16_f32 v23, v24, v25
	s_nop 1
	v_addc_co_u32_e32 v79, vcc, 0, v111, vcc
	global_store_dwordx4 v[78:79], v[86:89], off sc1
	v_cvt_pk_bf16_f32 v78, v82, v83
	v_cvt_pk_bf16_f32 v79, v84, v85
	ds_write_b128 v131, v[78:81]
	ds_write_b128 v126, v[70:73]
	ds_read_b128 v[66:69], v130
	ds_read_b128 v[70:73], v130 offset:1024
	v_add_co_u32_e32 v74, vcc, s63, v110
	ds_write_b128 v131, v[62:65]
	s_nop 0
	v_addc_co_u32_e32 v75, vcc, 0, v111, vcc
	s_waitcnt lgkmcnt(0)
	global_store_dwordx4 v[74:75], v[66:69], off sc1
	ds_write_b128 v126, v[54:57]
	v_cvt_pk_bf16_f32 v24, v14, v15
	v_cvt_pk_bf16_f32 v25, v16, v17
	v_cvt_pk_bf16_f32 v6, v6, v7
	v_cvt_pk_bf16_f32 v7, v8, v9
	s_nop 0
	v_add_co_u32_e32 v66, vcc, s64, v110
	v_cvt_pk_bf16_f32 v8, v2, v3
	v_cvt_pk_bf16_f32 v9, v4, v5
	s_mov_b64 s[0:1], -1
	s_nop 0
	v_addc_co_u32_e32 v67, vcc, 0, v111, vcc
	global_store_dwordx4 v[66:67], v[70:73], off sc1
	ds_read_b128 v[46:49], v130
	ds_read_b128 v[54:57], v130 offset:1024
	v_add_co_u32_e32 v58, vcc, s65, v110
	s_nop 1
	v_addc_co_u32_e32 v59, vcc, 0, v111, vcc
	s_waitcnt lgkmcnt(0)
	global_store_dwordx4 v[58:59], v[46:49], off sc1
	s_nop 1
	v_add_co_u32_e32 v46, vcc, s66, v110
	v_cvt_pk_bf16_f32 v48, v42, v43
	v_cvt_pk_bf16_f32 v49, v44, v45
	s_nop 1
	v_addc_co_u32_e32 v47, vcc, 0, v111, vcc
	global_store_dwordx4 v[46:47], v[54:57], off sc1
	v_cvt_pk_bf16_f32 v46, v50, v51
	v_cvt_pk_bf16_f32 v47, v52, v53
	ds_write_b128 v131, v[46:49]
	ds_write_b128 v126, v[38:41]
	ds_read_b128 v[30:33], v130
	ds_read_b128 v[38:41], v130 offset:1024
	v_add_co_u32_e32 v42, vcc, s67, v110
	s_nop 1
	v_addc_co_u32_e32 v43, vcc, 0, v111, vcc
	s_waitcnt lgkmcnt(0)
	global_store_dwordx4 v[42:43], v[30:33], off sc1
	s_nop 1
	v_add_co_u32_e32 v30, vcc, s68, v110
	v_cvt_pk_bf16_f32 v32, v26, v27
	v_cvt_pk_bf16_f32 v33, v28, v29
	s_nop 1
	v_addc_co_u32_e32 v31, vcc, 0, v111, vcc
	global_store_dwordx4 v[30:31], v[38:41], off sc1
	v_cvt_pk_bf16_f32 v30, v34, v35
	v_cvt_pk_bf16_f32 v31, v36, v37
	ds_write_b128 v131, v[30:33]
	ds_write_b128 v126, v[22:25]
	ds_read_b128 v[14:17], v130
	ds_read_b128 v[22:25], v130 offset:1024
	v_add_co_u32_e32 v26, vcc, s69, v110
	s_nop 1
	v_addc_co_u32_e32 v27, vcc, 0, v111, vcc
	s_waitcnt lgkmcnt(0)
	global_store_dwordx4 v[26:27], v[14:17], off sc1
	s_nop 1
	v_add_co_u32_e32 v14, vcc, s70, v110
	v_cvt_pk_bf16_f32 v16, v10, v11
	v_cvt_pk_bf16_f32 v17, v12, v13
	s_nop 1
	v_addc_co_u32_e32 v15, vcc, 0, v111, vcc
	global_store_dwordx4 v[14:15], v[22:25], off sc1
	v_cvt_pk_bf16_f32 v14, v18, v19
	v_cvt_pk_bf16_f32 v15, v20, v21
	ds_write_b128 v131, v[14:17]
	ds_write_b128 v126, v[6:9]
	ds_read_b128 v[2:5], v130
	ds_read_b128 v[6:9], v130 offset:1024
	v_add_co_u32_e32 v10, vcc, 0x688000, v110
	s_nop 1
	v_addc_co_u32_e32 v11, vcc, 0, v111, vcc
	s_waitcnt lgkmcnt(0)
	global_store_dwordx4 v[10:11], v[2:5], off sc1
	s_nop 1
	v_add_co_u32_e32 v2, vcc, 0x6d4000, v110
	s_nop 1
	v_addc_co_u32_e32 v3, vcc, 0, v111, vcc
	s_andn2_b64 vcc, exec, s[22:23]
	global_store_dwordx4 v[2:3], v[6:9], off sc1
	s_cbranch_vccnz .LBB0_203
	s_andn2_b64 vcc, exec, s[8:9]
	s_cbranch_vccnz .LBB0_202
	s_barrier
	s_branch .LBB0_202

.LBB0_348:
	v_mov_b32_e32 v130, v183
	v_cvt_pk_bf16_f32 v126, v126, v127
	v_cvt_pk_bf16_f32 v127, v128, v129
	v_cvt_pk_bf16_f32 v128, v122, v123
	v_cvt_pk_bf16_f32 v129, v124, v125
	v_cvt_pk_bf16_f32 v118, v118, v119
	s_nop 0
	v_and_b32_e32 v132, 7, v130
	v_lshlrev_b32_e32 v133, 7, v130
	v_lshrrev_b32_e32 v134, 3, v130
	v_and_b32_e32 v133, 0x780, v133
	v_bitop3_b32 v134, v134, v132, s65 bitop3:0x6c
	v_ashrrev_i32_e32 v131, 3, v130
	v_add_u32_e32 v133, s39, v133
	v_lshlrev_b32_e32 v134, 4, v134
	v_lshlrev_b32_e32 v135, 7, v131
	v_bitop3_b32 v130, v130, v131, 7 bitop3:0x6c
	v_add_u32_e32 v131, v133, v134
	v_lshlrev_b32_e32 v130, 4, v130
	ds_write_b128 v131, v[126:129]
	v_xad_u32 v126, v134, 16, v133
	v_add3_u32 v130, s39, v135, v130
	v_cvt_pk_bf16_f32 v119, v120, v121
	v_cvt_pk_bf16_f32 v120, v110, v111
	v_cvt_pk_bf16_f32 v121, v112, v113
	ds_write_b128 v126, v[118:121]
	ds_read_b128 v[118:121], v130
	ds_read_b128 v[122:125], v130 offset:1024
	v_lshl_or_b32 v112, v132, 4, s59
	v_mov_b32_e32 v113, v173
	v_lshl_add_u64 v[110:111], s[4:5], 0, v[112:113]
	s_waitcnt lgkmcnt(0)
	global_store_dwordx4 v112, v[118:121], s[4:5] sc1
	v_add_co_u32_e32 v112, vcc, s66, v110
	v_cvt_pk_bf16_f32 v102, v102, v103
	v_cvt_pk_bf16_f32 v103, v104, v105
	v_cvt_pk_bf16_f32 v104, v94, v95
	v_cvt_pk_bf16_f32 v105, v96, v97
	s_nop 1
	v_addc_co_u32_e32 v113, vcc, 0, v111, vcc
	global_store_dwordx4 v[112:113], v[122:125], off sc1
	v_cvt_pk_bf16_f32 v112, v114, v115
	v_cvt_pk_bf16_f32 v113, v116, v117
	v_cvt_pk_bf16_f32 v114, v106, v107
	v_cvt_pk_bf16_f32 v115, v108, v109
	ds_write_b128 v131, v[112:115]
	ds_write_b128 v126, v[102:105]
	ds_read_b128 v[94:97], v130
	ds_read_b128 v[102:105], v130 offset:1024
	v_add_co_u32_e32 v106, vcc, s67, v110
	v_cvt_pk_bf16_f32 v86, v86, v87
	v_cvt_pk_bf16_f32 v87, v88, v89
	v_cvt_pk_bf16_f32 v88, v78, v79
	v_cvt_pk_bf16_f32 v89, v80, v81
	s_nop 1
	v_addc_co_u32_e32 v107, vcc, 0, v111, vcc
	s_waitcnt lgkmcnt(0)
	global_store_dwordx4 v[106:107], v[94:97], off sc1
	v_cvt_pk_bf16_f32 v70, v70, v71
	v_cvt_pk_bf16_f32 v71, v72, v73
	v_cvt_pk_bf16_f32 v72, v66, v67
	v_cvt_pk_bf16_f32 v73, v68, v69
	v_cvt_pk_bf16_f32 v62, v62, v63
	s_nop 1
	v_add_co_u32_e32 v94, vcc, s68, v110
	v_cvt_pk_bf16_f32 v96, v90, v91
	v_cvt_pk_bf16_f32 v97, v92, v93
	v_cvt_pk_bf16_f32 v63, v64, v65
	v_cvt_pk_bf16_f32 v64, v58, v59
	s_nop 1
	v_addc_co_u32_e32 v95, vcc, 0, v111, vcc
	global_store_dwordx4 v[94:95], v[102:105], off sc1
	v_cvt_pk_bf16_f32 v94, v98, v99
	v_cvt_pk_bf16_f32 v95, v100, v101
	ds_write_b128 v131, v[94:97]
	ds_write_b128 v126, v[86:89]
	ds_read_b128 v[78:81], v130
	ds_read_b128 v[86:89], v130 offset:1024
	v_add_co_u32_e32 v90, vcc, s69, v110
	v_cvt_pk_bf16_f32 v65, v60, v61
	v_cvt_pk_bf16_f32 v54, v54, v55
	v_cvt_pk_bf16_f32 v55, v56, v57
	v_cvt_pk_bf16_f32 v56, v46, v47
	s_nop 1
	v_addc_co_u32_e32 v91, vcc, 0, v111, vcc
	s_waitcnt lgkmcnt(0)
	global_store_dwordx4 v[90:91], v[78:81], off sc1
	v_cvt_pk_bf16_f32 v57, v48, v49
	v_cvt_pk_bf16_f32 v38, v38, v39
	v_cvt_pk_bf16_f32 v39, v40, v41
	v_cvt_pk_bf16_f32 v40, v30, v31
	v_cvt_pk_bf16_f32 v41, v32, v33
	s_nop 1
	v_add_co_u32_e32 v78, vcc, s70, v110
	v_cvt_pk_bf16_f32 v80, v74, v75
	v_cvt_pk_bf16_f32 v81, v76, v77
	v_cvt_pk_bf16_f32 v22, v22, v23
	v_cvt_pk_bf16_f32 v23, v24, v25
	s_nop 1
	v_addc_co_u32_e32 v79, vcc, 0, v111, vcc
	global_store_dwordx4 v[78:79], v[86:89], off sc1
	v_cvt_pk_bf16_f32 v78, v82, v83
	v_cvt_pk_bf16_f32 v79, v84, v85
	ds_write_b128 v131, v[78:81]
	ds_write_b128 v126, v[70:73]
	ds_read_b128 v[66:69], v130
	ds_read_b128 v[70:73], v130 offset:1024
	v_add_co_u32_e32 v74, vcc, s71, v110
	ds_write_b128 v131, v[62:65]
	s_nop 0
	v_addc_co_u32_e32 v75, vcc, 0, v111, vcc
	s_waitcnt lgkmcnt(0)
	global_store_dwordx4 v[74:75], v[66:69], off sc1
	ds_write_b128 v126, v[54:57]
	v_cvt_pk_bf16_f32 v24, v14, v15
	v_cvt_pk_bf16_f32 v25, v16, v17
	v_cvt_pk_bf16_f32 v6, v6, v7
	v_cvt_pk_bf16_f32 v7, v8, v9
	s_nop 0
	v_add_co_u32_e32 v66, vcc, s72, v110
	v_cvt_pk_bf16_f32 v8, v2, v3
	v_cvt_pk_bf16_f32 v9, v4, v5
	s_mov_b64 s[0:1], -1
	s_nop 0
	v_addc_co_u32_e32 v67, vcc, 0, v111, vcc
	global_store_dwordx4 v[66:67], v[70:73], off sc1
	ds_read_b128 v[46:49], v130
	ds_read_b128 v[54:57], v130 offset:1024
	v_add_co_u32_e32 v58, vcc, s73, v110
	s_nop 1
	v_addc_co_u32_e32 v59, vcc, 0, v111, vcc
	s_waitcnt lgkmcnt(0)
	global_store_dwordx4 v[58:59], v[46:49], off sc1
	s_nop 1
	v_add_co_u32_e32 v46, vcc, s74, v110
	v_cvt_pk_bf16_f32 v48, v42, v43
	v_cvt_pk_bf16_f32 v49, v44, v45
	s_nop 1
	v_addc_co_u32_e32 v47, vcc, 0, v111, vcc
	global_store_dwordx4 v[46:47], v[54:57], off sc1
	v_cvt_pk_bf16_f32 v46, v50, v51
	v_cvt_pk_bf16_f32 v47, v52, v53
	ds_write_b128 v131, v[46:49]
	ds_write_b128 v126, v[38:41]
	ds_read_b128 v[30:33], v130
	ds_read_b128 v[38:41], v130 offset:1024
	v_add_co_u32_e32 v42, vcc, s75, v110
	s_nop 1
	v_addc_co_u32_e32 v43, vcc, 0, v111, vcc
	s_waitcnt lgkmcnt(0)
	global_store_dwordx4 v[42:43], v[30:33], off sc1
	s_nop 1
	v_add_co_u32_e32 v30, vcc, s76, v110
	v_cvt_pk_bf16_f32 v32, v26, v27
	v_cvt_pk_bf16_f32 v33, v28, v29
	s_nop 1
	v_addc_co_u32_e32 v31, vcc, 0, v111, vcc
	global_store_dwordx4 v[30:31], v[38:41], off sc1
	v_cvt_pk_bf16_f32 v30, v34, v35
	v_cvt_pk_bf16_f32 v31, v36, v37
	ds_write_b128 v131, v[30:33]
	ds_write_b128 v126, v[22:25]
	ds_read_b128 v[14:17], v130
	ds_read_b128 v[22:25], v130 offset:1024
	v_add_co_u32_e32 v26, vcc, s77, v110
	s_nop 1
	v_addc_co_u32_e32 v27, vcc, 0, v111, vcc
	s_waitcnt lgkmcnt(0)
	global_store_dwordx4 v[26:27], v[14:17], off sc1
	s_nop 1
	v_add_co_u32_e32 v14, vcc, s78, v110
	v_cvt_pk_bf16_f32 v16, v10, v11
	v_cvt_pk_bf16_f32 v17, v12, v13
	s_nop 1
	v_addc_co_u32_e32 v15, vcc, 0, v111, vcc
	global_store_dwordx4 v[14:15], v[22:25], off sc1
	v_cvt_pk_bf16_f32 v14, v18, v19
	v_cvt_pk_bf16_f32 v15, v20, v21
	ds_write_b128 v131, v[14:17]
	ds_write_b128 v126, v[6:9]
	ds_read_b128 v[2:5], v130
	ds_read_b128 v[6:9], v130 offset:1024
	v_add_co_u32_e32 v10, vcc, 0x688000, v110
	s_nop 1
	v_addc_co_u32_e32 v11, vcc, 0, v111, vcc
	s_waitcnt lgkmcnt(0)
	global_store_dwordx4 v[10:11], v[2:5], off sc1
	s_nop 1
	v_add_co_u32_e32 v2, vcc, 0x6d4000, v110
	s_nop 1
	v_addc_co_u32_e32 v3, vcc, 0, v111, vcc
	s_andn2_b64 vcc, exec, s[26:27]
	global_store_dwordx4 v[2:3], v[6:9], off sc1
	s_cbranch_vccnz .LBB0_336
	s_andn2_b64 vcc, exec, s[16:17]
	s_cbranch_vccnz .LBB0_335
	s_barrier
	s_branch .LBB0_335

.LBB0_372:
	v_mov_b32_e32 v2, v210
	s_nop 15
	s_nop 15
	s_nop 15
	s_add_i32 s0, s65, s56
	v_lshlrev_b32_e32 v5, 7, v2
	v_and_b32_e32 v5, 0x780, v5
	v_ashrrev_i32_e32 v3, 3, v2
	v_and_b32_e32 v4, 7, v2
	v_add_u32_e32 v10, s39, v5
	v_lshrrev_b32_e32 v5, 3, v2
	v_bitop3_b32 v5, v5, v4, s60 bitop3:0x6c
	v_bitop3_b32 v2, v2, v3, 7 bitop3:0x6c
	v_lshlrev_b32_e32 v11, 4, v5
	v_lshlrev_b32_e32 v5, 7, v3
	v_lshlrev_b32_e32 v2, 4, v2
	v_add3_u32 v16, s39, v5, v2
	v_lshl_or_b32 v2, v4, 4, s59
	v_add_u32_e32 v13, s0, v3
	v_lshl_or_b32 v12, s66, 9, v2
	v_pk_mul_f32 v[4:5], v[160:161], s[18:19] op_sel_hi:[1,0]
	v_pk_mul_f32 v[2:3], v[158:159], s[18:19] op_sel_hi:[1,0]
	v_pk_mul_f32 v[6:7], v[156:157], s[18:19] op_sel_hi:[1,0]
	v_pk_mul_f32 v[8:9], v[154:155], s[18:19] op_sel_hi:[1,0]
	v_cvt_pk_bf16_f32 v2, v2, v3
	v_cvt_pk_bf16_f32 v3, v4, v5
	v_cvt_pk_bf16_f32 v5, v6, v7
	v_add_u32_e32 v17, v10, v11
	v_cvt_pk_bf16_f32 v4, v8, v9
	ds_write_b128 v17, v[2:5]
	v_pk_mul_f32 v[4:5], v[152:153], s[18:19] op_sel_hi:[1,0]
	v_pk_mul_f32 v[2:3], v[150:151], s[18:19] op_sel_hi:[1,0]
	v_xad_u32 v18, v11, 16, v10
	v_pk_mul_f32 v[6:7], v[148:149], s[18:19] op_sel_hi:[1,0]
	v_pk_mul_f32 v[8:9], v[146:147], s[18:19] op_sel_hi:[1,0]
	v_cvt_pk_bf16_f32 v2, v2, v3
	v_cvt_pk_bf16_f32 v3, v4, v5
	v_cvt_pk_bf16_f32 v5, v6, v7
	s_nop 0
	v_cvt_pk_bf16_f32 v4, v8, v9
	ds_write_b128 v18, v[2:5]
	ds_read_b128 v[4:7], v16
	ds_read_b128 v[8:11], v16 offset:1024
	v_mad_u64_u32 v[2:3], s[0:1], v13, s61, v[12:13]
	v_mov_b32_e32 v3, v173
	v_lshl_add_u64 v[12:13], s[4:5], 0, v[2:3]
	s_waitcnt lgkmcnt(0)
	global_store_dwordx4 v2, v[4:7], s[4:5] sc1
	s_mov_b64 s[0:1], -1
	s_nop 0
	v_add_co_u32_e32 v4, vcc, s62, v12
	v_pk_mul_f32 v[6:7], v[144:145], s[18:19] op_sel_hi:[1,0]
	s_nop 0
	v_addc_co_u32_e32 v5, vcc, 0, v13, vcc
	global_store_dwordx4 v[4:5], v[8:11], off sc1
	v_pk_mul_f32 v[4:5], v[142:143], s[18:19] op_sel_hi:[1,0]
	v_add_u32_e32 v12, 0x98000, v2
	v_pk_mul_f32 v[8:9], v[140:141], s[18:19] op_sel_hi:[1,0]
	v_pk_mul_f32 v[10:11], v[138:139], s[18:19] op_sel_hi:[1,0]
	v_cvt_pk_bf16_f32 v4, v4, v5
	v_cvt_pk_bf16_f32 v5, v6, v7
	v_cvt_pk_bf16_f32 v7, v8, v9
	v_pk_mul_f32 v[8:9], v[132:133], s[18:19] op_sel_hi:[1,0]
	v_cvt_pk_bf16_f32 v6, v10, v11
	ds_write_b128 v17, v[4:7]
	v_pk_mul_f32 v[6:7], v[136:137], s[18:19] op_sel_hi:[1,0]
	v_pk_mul_f32 v[4:5], v[134:135], s[18:19] op_sel_hi:[1,0]
	v_pk_mul_f32 v[10:11], v[130:131], s[18:19] op_sel_hi:[1,0]
	v_cvt_pk_bf16_f32 v4, v4, v5
	v_cvt_pk_bf16_f32 v5, v6, v7
	v_cvt_pk_bf16_f32 v7, v8, v9
	v_mov_b32_e32 v13, v173
	v_cvt_pk_bf16_f32 v6, v10, v11
	ds_write_b128 v18, v[4:7]
	ds_read_b128 v[4:7], v16
	ds_read_b128 v[8:11], v16 offset:1024
	v_lshl_add_u64 v[14:15], s[4:5], 0, v[12:13]
	s_waitcnt lgkmcnt(0)
	global_store_dwordx4 v12, v[4:7], s[4:5] sc1
	s_nop 1
	v_add_co_u32_e32 v4, vcc, s62, v14
	v_pk_mul_f32 v[6:7], v[128:129], s[18:19] op_sel_hi:[1,0]
	s_nop 0
	v_addc_co_u32_e32 v5, vcc, 0, v15, vcc
	global_store_dwordx4 v[4:5], v[8:11], off sc1
	v_pk_mul_f32 v[4:5], v[126:127], s[18:19] op_sel_hi:[1,0]
	v_add_u32_e32 v12, 0x130000, v2
	v_pk_mul_f32 v[8:9], v[124:125], s[18:19] op_sel_hi:[1,0]
	v_pk_mul_f32 v[10:11], v[122:123], s[18:19] op_sel_hi:[1,0]
	v_cvt_pk_bf16_f32 v4, v4, v5
	v_cvt_pk_bf16_f32 v5, v6, v7
	v_cvt_pk_bf16_f32 v7, v8, v9
	v_pk_mul_f32 v[8:9], v[116:117], s[18:19] op_sel_hi:[1,0]
	v_cvt_pk_bf16_f32 v6, v10, v11
	ds_write_b128 v17, v[4:7]
	v_pk_mul_f32 v[6:7], v[120:121], s[18:19] op_sel_hi:[1,0]
	v_pk_mul_f32 v[4:5], v[118:119], s[18:19] op_sel_hi:[1,0]
	v_pk_mul_f32 v[10:11], v[114:115], s[18:19] op_sel_hi:[1,0]
	v_cvt_pk_bf16_f32 v4, v4, v5
	v_cvt_pk_bf16_f32 v5, v6, v7
	v_cvt_pk_bf16_f32 v7, v8, v9
	v_lshl_add_u64 v[14:15], s[4:5], 0, v[12:13]
	v_cvt_pk_bf16_f32 v6, v10, v11
	ds_write_b128 v18, v[4:7]
	ds_read_b128 v[4:7], v16
	ds_read_b128 v[8:11], v16 offset:1024
	s_waitcnt lgkmcnt(0)
	global_store_dwordx4 v12, v[4:7], s[4:5] sc1
	s_nop 1
	v_add_co_u32_e32 v4, vcc, s62, v14
	v_pk_mul_f32 v[6:7], v[112:113], s[18:19] op_sel_hi:[1,0]
	s_nop 0
	v_addc_co_u32_e32 v5, vcc, 0, v15, vcc
	global_store_dwordx4 v[4:5], v[8:11], off sc1
	v_pk_mul_f32 v[4:5], v[110:111], s[18:19] op_sel_hi:[1,0]
	v_add_u32_e32 v12, 0x1c8000, v2
	v_pk_mul_f32 v[8:9], v[108:109], s[18:19] op_sel_hi:[1,0]
	v_pk_mul_f32 v[10:11], v[106:107], s[18:19] op_sel_hi:[1,0]
	v_cvt_pk_bf16_f32 v4, v4, v5
	v_cvt_pk_bf16_f32 v5, v6, v7
	v_cvt_pk_bf16_f32 v7, v8, v9
	v_pk_mul_f32 v[8:9], v[100:101], s[18:19] op_sel_hi:[1,0]
	v_cvt_pk_bf16_f32 v6, v10, v11
	ds_write_b128 v17, v[4:7]
	v_pk_mul_f32 v[6:7], v[104:105], s[18:19] op_sel_hi:[1,0]
	v_pk_mul_f32 v[4:5], v[102:103], s[18:19] op_sel_hi:[1,0]
	v_pk_mul_f32 v[10:11], v[98:99], s[18:19] op_sel_hi:[1,0]
	v_cvt_pk_bf16_f32 v4, v4, v5
	v_cvt_pk_bf16_f32 v5, v6, v7
	v_cvt_pk_bf16_f32 v7, v8, v9
	v_lshl_add_u64 v[14:15], s[4:5], 0, v[12:13]
	v_cvt_pk_bf16_f32 v6, v10, v11
	ds_write_b128 v18, v[4:7]
	ds_read_b128 v[4:7], v16
	ds_read_b128 v[8:11], v16 offset:1024
	s_waitcnt lgkmcnt(0)
	global_store_dwordx4 v12, v[4:7], s[4:5] sc1
	s_nop 1
	v_add_co_u32_e32 v4, vcc, s62, v14
	v_pk_mul_f32 v[6:7], v[96:97], s[18:19] op_sel_hi:[1,0]
	s_nop 0
	v_addc_co_u32_e32 v5, vcc, 0, v15, vcc
	global_store_dwordx4 v[4:5], v[8:11], off sc1
	v_pk_mul_f32 v[4:5], v[94:95], s[18:19] op_sel_hi:[1,0]
	v_add_u32_e32 v12, 0x4c0000, v2
	v_pk_mul_f32 v[8:9], v[92:93], s[18:19] op_sel_hi:[1,0]
	v_pk_mul_f32 v[10:11], v[90:91], s[18:19] op_sel_hi:[1,0]
	v_cvt_pk_bf16_f32 v4, v4, v5
	v_cvt_pk_bf16_f32 v5, v6, v7
	v_cvt_pk_bf16_f32 v7, v8, v9
	v_pk_mul_f32 v[8:9], v[84:85], s[18:19] op_sel_hi:[1,0]
	v_cvt_pk_bf16_f32 v6, v10, v11
	ds_write_b128 v17, v[4:7]
	v_pk_mul_f32 v[6:7], v[88:89], s[18:19] op_sel_hi:[1,0]
	v_pk_mul_f32 v[4:5], v[86:87], s[18:19] op_sel_hi:[1,0]
	v_pk_mul_f32 v[10:11], v[82:83], s[18:19] op_sel_hi:[1,0]
	v_cvt_pk_bf16_f32 v4, v4, v5
	v_cvt_pk_bf16_f32 v5, v6, v7
	v_cvt_pk_bf16_f32 v7, v8, v9
	v_lshl_add_u64 v[14:15], s[4:5], 0, v[12:13]
	v_cvt_pk_bf16_f32 v6, v10, v11
	ds_write_b128 v18, v[4:7]
	ds_read_b128 v[4:7], v16
	ds_read_b128 v[8:11], v16 offset:1024
	s_waitcnt lgkmcnt(0)
	global_store_dwordx4 v12, v[4:7], s[4:5] sc1
	s_nop 1
	v_add_co_u32_e32 v4, vcc, s62, v14
	v_pk_mul_f32 v[6:7], v[80:81], s[18:19] op_sel_hi:[1,0]
	s_nop 0
	v_addc_co_u32_e32 v5, vcc, 0, v15, vcc
	global_store_dwordx4 v[4:5], v[8:11], off sc1
	v_pk_mul_f32 v[4:5], v[78:79], s[18:19] op_sel_hi:[1,0]
	v_add_u32_e32 v12, 0x558000, v2
	v_pk_mul_f32 v[8:9], v[76:77], s[18:19] op_sel_hi:[1,0]
	v_pk_mul_f32 v[10:11], v[74:75], s[18:19] op_sel_hi:[1,0]
	v_cvt_pk_bf16_f32 v4, v4, v5
	v_cvt_pk_bf16_f32 v5, v6, v7
	v_cvt_pk_bf16_f32 v7, v8, v9
	v_pk_mul_f32 v[8:9], v[68:69], s[18:19] op_sel_hi:[1,0]
	v_cvt_pk_bf16_f32 v6, v10, v11
	ds_write_b128 v17, v[4:7]
	v_pk_mul_f32 v[6:7], v[72:73], s[18:19] op_sel_hi:[1,0]
	v_pk_mul_f32 v[4:5], v[70:71], s[18:19] op_sel_hi:[1,0]
	v_pk_mul_f32 v[10:11], v[66:67], s[18:19] op_sel_hi:[1,0]
	v_cvt_pk_bf16_f32 v4, v4, v5
	v_cvt_pk_bf16_f32 v5, v6, v7
	v_cvt_pk_bf16_f32 v7, v8, v9
	v_lshl_add_u64 v[14:15], s[4:5], 0, v[12:13]
	v_cvt_pk_bf16_f32 v6, v10, v11
	ds_write_b128 v18, v[4:7]
	ds_read_b128 v[4:7], v16
	ds_read_b128 v[8:11], v16 offset:1024
	s_waitcnt lgkmcnt(0)
	global_store_dwordx4 v12, v[4:7], s[4:5] sc1
	s_nop 1
	v_add_co_u32_e32 v4, vcc, s62, v14
	v_pk_mul_f32 v[6:7], v[64:65], s[18:19] op_sel_hi:[1,0]
	s_nop 0
	v_addc_co_u32_e32 v5, vcc, 0, v15, vcc
	global_store_dwordx4 v[4:5], v[8:11], off sc1
	v_pk_mul_f32 v[4:5], v[62:63], s[18:19] op_sel_hi:[1,0]
	v_add_u32_e32 v12, 0x5f0000, v2
	v_pk_mul_f32 v[8:9], v[60:61], s[18:19] op_sel_hi:[1,0]
	v_pk_mul_f32 v[10:11], v[58:59], s[18:19] op_sel_hi:[1,0]
	v_cvt_pk_bf16_f32 v4, v4, v5
	v_cvt_pk_bf16_f32 v5, v6, v7
	v_cvt_pk_bf16_f32 v7, v8, v9
	v_pk_mul_f32 v[8:9], v[52:53], s[18:19] op_sel_hi:[1,0]
	v_cvt_pk_bf16_f32 v6, v10, v11
	ds_write_b128 v17, v[4:7]
	v_pk_mul_f32 v[6:7], v[56:57], s[18:19] op_sel_hi:[1,0]
	v_pk_mul_f32 v[4:5], v[54:55], s[18:19] op_sel_hi:[1,0]
	v_pk_mul_f32 v[10:11], v[50:51], s[18:19] op_sel_hi:[1,0]
	v_cvt_pk_bf16_f32 v4, v4, v5
	v_cvt_pk_bf16_f32 v5, v6, v7
	v_cvt_pk_bf16_f32 v7, v8, v9
	v_lshl_add_u64 v[14:15], s[4:5], 0, v[12:13]
	v_cvt_pk_bf16_f32 v6, v10, v11
	ds_write_b128 v18, v[4:7]
	ds_read_b128 v[4:7], v16
	ds_read_b128 v[8:11], v16 offset:1024
	v_add_u32_e32 v2, 0x688000, v2
	s_waitcnt lgkmcnt(0)
	global_store_dwordx4 v12, v[4:7], s[4:5] sc1
	s_nop 1
	v_add_co_u32_e32 v4, vcc, s62, v14
	v_pk_mul_f32 v[6:7], v[48:49], s[18:19] op_sel_hi:[1,0]
	s_nop 0
	v_addc_co_u32_e32 v5, vcc, 0, v15, vcc
	global_store_dwordx4 v[4:5], v[8:11], off sc1
	v_pk_mul_f32 v[4:5], v[46:47], s[18:19] op_sel_hi:[1,0]
	v_lshl_add_u64 v[12:13], s[4:5], 0, v[2:3]
	v_pk_mul_f32 v[8:9], v[44:45], s[18:19] op_sel_hi:[1,0]
	v_pk_mul_f32 v[10:11], v[42:43], s[18:19] op_sel_hi:[1,0]
	v_cvt_pk_bf16_f32 v4, v4, v5
	v_cvt_pk_bf16_f32 v5, v6, v7
	v_cvt_pk_bf16_f32 v7, v8, v9
	v_pk_mul_f32 v[8:9], v[36:37], s[18:19] op_sel_hi:[1,0]
	v_cvt_pk_bf16_f32 v6, v10, v11
	ds_write_b128 v17, v[4:7]
	v_pk_mul_f32 v[6:7], v[40:41], s[18:19] op_sel_hi:[1,0]
	v_pk_mul_f32 v[4:5], v[38:39], s[18:19] op_sel_hi:[1,0]
	v_pk_mul_f32 v[10:11], v[34:35], s[18:19] op_sel_hi:[1,0]
	v_cvt_pk_bf16_f32 v4, v4, v5
	v_cvt_pk_bf16_f32 v5, v6, v7
	v_cvt_pk_bf16_f32 v7, v8, v9
	s_nop 0
	v_cvt_pk_bf16_f32 v6, v10, v11
	ds_write_b128 v18, v[4:7]
	ds_read_b128 v[4:7], v16
	ds_read_b128 v[8:11], v16 offset:1024
	s_waitcnt lgkmcnt(0)
	global_store_dwordx4 v2, v[4:7], s[4:5] sc1
	v_add_co_u32_e32 v2, vcc, 0x4c000, v12
	s_nop 1
	v_addc_co_u32_e32 v3, vcc, 0, v13, vcc
	s_andn2_b64 vcc, exec, s[24:25]
	global_store_dwordx4 v[2:3], v[8:11], off sc1
	s_cbranch_vccnz .LBB0_358
	s_andn2_b64 vcc, exec, s[10:11]
	s_cbranch_vccnz .LBB0_357
	s_barrier
	s_branch .LBB0_357

.LBB0_619:
	v_mov_b32_e32 v2, v197
	s_nop 15
	s_nop 15
	s_nop 15
	s_add_i32 s0, s63, s54
	v_lshlrev_b32_e32 v5, 7, v2
	v_and_b32_e32 v5, 0x780, v5
	v_ashrrev_i32_e32 v3, 3, v2
	v_and_b32_e32 v4, 7, v2
	v_add_u32_e32 v10, s39, v5
	v_lshrrev_b32_e32 v5, 3, v2
	v_bitop3_b32 v5, v5, v4, s58 bitop3:0x6c
	v_bitop3_b32 v2, v2, v3, 7 bitop3:0x6c
	v_lshlrev_b32_e32 v11, 4, v5
	v_lshlrev_b32_e32 v5, 7, v3
	v_lshlrev_b32_e32 v2, 4, v2
	v_add3_u32 v16, s39, v5, v2
	v_lshl_or_b32 v2, v4, 4, s57
	v_add_u32_e32 v13, s0, v3
	v_lshl_or_b32 v12, s24, 9, v2
	v_pk_mul_f32 v[4:5], v[160:161], s[16:17] op_sel_hi:[1,0]
	v_pk_mul_f32 v[2:3], v[158:159], s[16:17] op_sel_hi:[1,0]
	v_pk_mul_f32 v[6:7], v[156:157], s[16:17] op_sel_hi:[1,0]
	v_pk_mul_f32 v[8:9], v[154:155], s[16:17] op_sel_hi:[1,0]
	v_cvt_pk_bf16_f32 v2, v2, v3
	v_cvt_pk_bf16_f32 v3, v4, v5
	v_cvt_pk_bf16_f32 v5, v6, v7
	v_add_u32_e32 v17, v10, v11
	v_cvt_pk_bf16_f32 v4, v8, v9
	ds_write_b128 v17, v[2:5]
	v_pk_mul_f32 v[4:5], v[152:153], s[16:17] op_sel_hi:[1,0]
	v_pk_mul_f32 v[2:3], v[150:151], s[16:17] op_sel_hi:[1,0]
	v_xad_u32 v18, v11, 16, v10
	v_pk_mul_f32 v[6:7], v[148:149], s[16:17] op_sel_hi:[1,0]
	v_pk_mul_f32 v[8:9], v[146:147], s[16:17] op_sel_hi:[1,0]
	v_cvt_pk_bf16_f32 v2, v2, v3
	v_cvt_pk_bf16_f32 v3, v4, v5
	v_cvt_pk_bf16_f32 v5, v6, v7
	s_nop 0
	v_cvt_pk_bf16_f32 v4, v8, v9
	ds_write_b128 v18, v[2:5]
	ds_read_b128 v[4:7], v16
	ds_read_b128 v[8:11], v16 offset:1024
	v_mad_u64_u32 v[2:3], s[0:1], v13, s59, v[12:13]
	v_mov_b32_e32 v3, v173
	v_lshl_add_u64 v[12:13], s[4:5], 0, v[2:3]
	s_waitcnt lgkmcnt(0)
	global_store_dwordx4 v2, v[4:7], s[4:5] sc1
	s_mov_b64 s[0:1], -1
	s_nop 0
	v_add_co_u32_e32 v4, vcc, s60, v12
	v_pk_mul_f32 v[6:7], v[144:145], s[16:17] op_sel_hi:[1,0]
	s_nop 0
	v_addc_co_u32_e32 v5, vcc, 0, v13, vcc
	global_store_dwordx4 v[4:5], v[8:11], off sc1
	v_pk_mul_f32 v[4:5], v[142:143], s[16:17] op_sel_hi:[1,0]
	v_add_u32_e32 v12, 0x98000, v2
	v_pk_mul_f32 v[8:9], v[140:141], s[16:17] op_sel_hi:[1,0]
	v_pk_mul_f32 v[10:11], v[138:139], s[16:17] op_sel_hi:[1,0]
	v_cvt_pk_bf16_f32 v4, v4, v5
	v_cvt_pk_bf16_f32 v5, v6, v7
	v_cvt_pk_bf16_f32 v7, v8, v9
	v_pk_mul_f32 v[8:9], v[132:133], s[16:17] op_sel_hi:[1,0]
	v_cvt_pk_bf16_f32 v6, v10, v11
	ds_write_b128 v17, v[4:7]
	v_pk_mul_f32 v[6:7], v[136:137], s[16:17] op_sel_hi:[1,0]
	v_pk_mul_f32 v[4:5], v[134:135], s[16:17] op_sel_hi:[1,0]
	v_pk_mul_f32 v[10:11], v[130:131], s[16:17] op_sel_hi:[1,0]
	v_cvt_pk_bf16_f32 v4, v4, v5
	v_cvt_pk_bf16_f32 v5, v6, v7
	v_cvt_pk_bf16_f32 v7, v8, v9
	v_mov_b32_e32 v13, v173
	v_cvt_pk_bf16_f32 v6, v10, v11
	ds_write_b128 v18, v[4:7]
	ds_read_b128 v[4:7], v16
	ds_read_b128 v[8:11], v16 offset:1024
	v_lshl_add_u64 v[14:15], s[4:5], 0, v[12:13]
	s_waitcnt lgkmcnt(0)
	global_store_dwordx4 v12, v[4:7], s[4:5] sc1
	s_nop 1
	v_add_co_u32_e32 v4, vcc, s60, v14
	v_pk_mul_f32 v[6:7], v[128:129], s[16:17] op_sel_hi:[1,0]
	s_nop 0
	v_addc_co_u32_e32 v5, vcc, 0, v15, vcc
	global_store_dwordx4 v[4:5], v[8:11], off sc1
	v_pk_mul_f32 v[4:5], v[126:127], s[16:17] op_sel_hi:[1,0]
	v_add_u32_e32 v12, 0x130000, v2
	v_pk_mul_f32 v[8:9], v[124:125], s[16:17] op_sel_hi:[1,0]
	v_pk_mul_f32 v[10:11], v[122:123], s[16:17] op_sel_hi:[1,0]
	v_cvt_pk_bf16_f32 v4, v4, v5
	v_cvt_pk_bf16_f32 v5, v6, v7
	v_cvt_pk_bf16_f32 v7, v8, v9
	v_pk_mul_f32 v[8:9], v[116:117], s[16:17] op_sel_hi:[1,0]
	v_cvt_pk_bf16_f32 v6, v10, v11
	ds_write_b128 v17, v[4:7]
	v_pk_mul_f32 v[6:7], v[120:121], s[16:17] op_sel_hi:[1,0]
	v_pk_mul_f32 v[4:5], v[118:119], s[16:17] op_sel_hi:[1,0]
	v_pk_mul_f32 v[10:11], v[114:115], s[16:17] op_sel_hi:[1,0]
	v_cvt_pk_bf16_f32 v4, v4, v5
	v_cvt_pk_bf16_f32 v5, v6, v7
	v_cvt_pk_bf16_f32 v7, v8, v9
	v_lshl_add_u64 v[14:15], s[4:5], 0, v[12:13]
	v_cvt_pk_bf16_f32 v6, v10, v11
	ds_write_b128 v18, v[4:7]
	ds_read_b128 v[4:7], v16
	ds_read_b128 v[8:11], v16 offset:1024
	s_waitcnt lgkmcnt(0)
	global_store_dwordx4 v12, v[4:7], s[4:5] sc1
	s_nop 1
	v_add_co_u32_e32 v4, vcc, s60, v14
	v_pk_mul_f32 v[6:7], v[112:113], s[16:17] op_sel_hi:[1,0]
	s_nop 0
	v_addc_co_u32_e32 v5, vcc, 0, v15, vcc
	global_store_dwordx4 v[4:5], v[8:11], off sc1
	v_pk_mul_f32 v[4:5], v[110:111], s[16:17] op_sel_hi:[1,0]
	v_add_u32_e32 v12, 0x1c8000, v2
	v_pk_mul_f32 v[8:9], v[108:109], s[16:17] op_sel_hi:[1,0]
	v_pk_mul_f32 v[10:11], v[106:107], s[16:17] op_sel_hi:[1,0]
	v_cvt_pk_bf16_f32 v4, v4, v5
	v_cvt_pk_bf16_f32 v5, v6, v7
	v_cvt_pk_bf16_f32 v7, v8, v9
	v_pk_mul_f32 v[8:9], v[100:101], s[16:17] op_sel_hi:[1,0]
	v_cvt_pk_bf16_f32 v6, v10, v11
	ds_write_b128 v17, v[4:7]
	v_pk_mul_f32 v[6:7], v[104:105], s[16:17] op_sel_hi:[1,0]
	v_pk_mul_f32 v[4:5], v[102:103], s[16:17] op_sel_hi:[1,0]
	v_pk_mul_f32 v[10:11], v[98:99], s[16:17] op_sel_hi:[1,0]
	v_cvt_pk_bf16_f32 v4, v4, v5
	v_cvt_pk_bf16_f32 v5, v6, v7
	v_cvt_pk_bf16_f32 v7, v8, v9
	v_lshl_add_u64 v[14:15], s[4:5], 0, v[12:13]
	v_cvt_pk_bf16_f32 v6, v10, v11
	ds_write_b128 v18, v[4:7]
	ds_read_b128 v[4:7], v16
	ds_read_b128 v[8:11], v16 offset:1024
	s_waitcnt lgkmcnt(0)
	global_store_dwordx4 v12, v[4:7], s[4:5] sc1
	s_nop 1
	v_add_co_u32_e32 v4, vcc, s60, v14
	v_pk_mul_f32 v[6:7], v[96:97], s[16:17] op_sel_hi:[1,0]
	s_nop 0
	v_addc_co_u32_e32 v5, vcc, 0, v15, vcc
	global_store_dwordx4 v[4:5], v[8:11], off sc1
	v_pk_mul_f32 v[4:5], v[94:95], s[16:17] op_sel_hi:[1,0]
	v_add_u32_e32 v12, 0x4c0000, v2
	v_pk_mul_f32 v[8:9], v[92:93], s[16:17] op_sel_hi:[1,0]
	v_pk_mul_f32 v[10:11], v[90:91], s[16:17] op_sel_hi:[1,0]
	v_cvt_pk_bf16_f32 v4, v4, v5
	v_cvt_pk_bf16_f32 v5, v6, v7
	v_cvt_pk_bf16_f32 v7, v8, v9
	v_pk_mul_f32 v[8:9], v[84:85], s[16:17] op_sel_hi:[1,0]
	v_cvt_pk_bf16_f32 v6, v10, v11
	ds_write_b128 v17, v[4:7]
	v_pk_mul_f32 v[6:7], v[88:89], s[16:17] op_sel_hi:[1,0]
	v_pk_mul_f32 v[4:5], v[86:87], s[16:17] op_sel_hi:[1,0]
	v_pk_mul_f32 v[10:11], v[82:83], s[16:17] op_sel_hi:[1,0]
	v_cvt_pk_bf16_f32 v4, v4, v5
	v_cvt_pk_bf16_f32 v5, v6, v7
	v_cvt_pk_bf16_f32 v7, v8, v9
	v_lshl_add_u64 v[14:15], s[4:5], 0, v[12:13]
	v_cvt_pk_bf16_f32 v6, v10, v11
	ds_write_b128 v18, v[4:7]
	ds_read_b128 v[4:7], v16
	ds_read_b128 v[8:11], v16 offset:1024
	s_waitcnt lgkmcnt(0)
	global_store_dwordx4 v12, v[4:7], s[4:5] sc1
	s_nop 1
	v_add_co_u32_e32 v4, vcc, s60, v14
	v_pk_mul_f32 v[6:7], v[80:81], s[16:17] op_sel_hi:[1,0]
	s_nop 0
	v_addc_co_u32_e32 v5, vcc, 0, v15, vcc
	global_store_dwordx4 v[4:5], v[8:11], off sc1
	v_pk_mul_f32 v[4:5], v[78:79], s[16:17] op_sel_hi:[1,0]
	v_add_u32_e32 v12, 0x558000, v2
	v_pk_mul_f32 v[8:9], v[76:77], s[16:17] op_sel_hi:[1,0]
	v_pk_mul_f32 v[10:11], v[74:75], s[16:17] op_sel_hi:[1,0]
	v_cvt_pk_bf16_f32 v4, v4, v5
	v_cvt_pk_bf16_f32 v5, v6, v7
	v_cvt_pk_bf16_f32 v7, v8, v9
	v_pk_mul_f32 v[8:9], v[68:69], s[16:17] op_sel_hi:[1,0]
	v_cvt_pk_bf16_f32 v6, v10, v11
	ds_write_b128 v17, v[4:7]
	v_pk_mul_f32 v[6:7], v[72:73], s[16:17] op_sel_hi:[1,0]
	v_pk_mul_f32 v[4:5], v[70:71], s[16:17] op_sel_hi:[1,0]
	v_pk_mul_f32 v[10:11], v[66:67], s[16:17] op_sel_hi:[1,0]
	v_cvt_pk_bf16_f32 v4, v4, v5
	v_cvt_pk_bf16_f32 v5, v6, v7
	v_cvt_pk_bf16_f32 v7, v8, v9
	v_lshl_add_u64 v[14:15], s[4:5], 0, v[12:13]
	v_cvt_pk_bf16_f32 v6, v10, v11
	ds_write_b128 v18, v[4:7]
	ds_read_b128 v[4:7], v16
	ds_read_b128 v[8:11], v16 offset:1024
	s_waitcnt lgkmcnt(0)
	global_store_dwordx4 v12, v[4:7], s[4:5] sc1
	s_nop 1
	v_add_co_u32_e32 v4, vcc, s60, v14
	v_pk_mul_f32 v[6:7], v[64:65], s[16:17] op_sel_hi:[1,0]
	s_nop 0
	v_addc_co_u32_e32 v5, vcc, 0, v15, vcc
	global_store_dwordx4 v[4:5], v[8:11], off sc1
	v_pk_mul_f32 v[4:5], v[62:63], s[16:17] op_sel_hi:[1,0]
	v_add_u32_e32 v12, 0x5f0000, v2
	v_pk_mul_f32 v[8:9], v[60:61], s[16:17] op_sel_hi:[1,0]
	v_pk_mul_f32 v[10:11], v[58:59], s[16:17] op_sel_hi:[1,0]
	v_cvt_pk_bf16_f32 v4, v4, v5
	v_cvt_pk_bf16_f32 v5, v6, v7
	v_cvt_pk_bf16_f32 v7, v8, v9
	v_pk_mul_f32 v[8:9], v[52:53], s[16:17] op_sel_hi:[1,0]
	v_cvt_pk_bf16_f32 v6, v10, v11
	ds_write_b128 v17, v[4:7]
	v_pk_mul_f32 v[6:7], v[56:57], s[16:17] op_sel_hi:[1,0]
	v_pk_mul_f32 v[4:5], v[54:55], s[16:17] op_sel_hi:[1,0]
	v_pk_mul_f32 v[10:11], v[50:51], s[16:17] op_sel_hi:[1,0]
	v_cvt_pk_bf16_f32 v4, v4, v5
	v_cvt_pk_bf16_f32 v5, v6, v7
	v_cvt_pk_bf16_f32 v7, v8, v9
	v_lshl_add_u64 v[14:15], s[4:5], 0, v[12:13]
	v_cvt_pk_bf16_f32 v6, v10, v11
	ds_write_b128 v18, v[4:7]
	ds_read_b128 v[4:7], v16
	ds_read_b128 v[8:11], v16 offset:1024
	v_add_u32_e32 v2, 0x688000, v2
	s_waitcnt lgkmcnt(0)
	global_store_dwordx4 v12, v[4:7], s[4:5] sc1
	s_nop 1
	v_add_co_u32_e32 v4, vcc, s60, v14
	v_pk_mul_f32 v[6:7], v[48:49], s[16:17] op_sel_hi:[1,0]
	s_nop 0
	v_addc_co_u32_e32 v5, vcc, 0, v15, vcc
	global_store_dwordx4 v[4:5], v[8:11], off sc1
	v_pk_mul_f32 v[4:5], v[46:47], s[16:17] op_sel_hi:[1,0]
	v_lshl_add_u64 v[12:13], s[4:5], 0, v[2:3]
	v_pk_mul_f32 v[8:9], v[44:45], s[16:17] op_sel_hi:[1,0]
	v_pk_mul_f32 v[10:11], v[42:43], s[16:17] op_sel_hi:[1,0]
	v_cvt_pk_bf16_f32 v4, v4, v5
	v_cvt_pk_bf16_f32 v5, v6, v7
	v_cvt_pk_bf16_f32 v7, v8, v9
	v_pk_mul_f32 v[8:9], v[36:37], s[16:17] op_sel_hi:[1,0]
	v_cvt_pk_bf16_f32 v6, v10, v11
	ds_write_b128 v17, v[4:7]
	v_pk_mul_f32 v[6:7], v[40:41], s[16:17] op_sel_hi:[1,0]
	v_pk_mul_f32 v[4:5], v[38:39], s[16:17] op_sel_hi:[1,0]
	v_pk_mul_f32 v[10:11], v[34:35], s[16:17] op_sel_hi:[1,0]
	v_cvt_pk_bf16_f32 v4, v4, v5
	v_cvt_pk_bf16_f32 v5, v6, v7
	v_cvt_pk_bf16_f32 v7, v8, v9
	s_nop 0
	v_cvt_pk_bf16_f32 v6, v10, v11
	ds_write_b128 v18, v[4:7]
	ds_read_b128 v[4:7], v16
	ds_read_b128 v[8:11], v16 offset:1024
	s_waitcnt lgkmcnt(0)
	global_store_dwordx4 v2, v[4:7], s[4:5] sc1
	v_add_co_u32_e32 v2, vcc, 0x4c000, v12
	s_nop 1
	v_addc_co_u32_e32 v3, vcc, 0, v13, vcc
	s_andn2_b64 vcc, exec, s[22:23]
	global_store_dwordx4 v[2:3], v[8:11], off sc1
	s_cbranch_vccnz .LBB0_605
	s_andn2_b64 vcc, exec, s[8:9]
	s_cbranch_vccnz .LBB0_604
	s_barrier
	s_branch .LBB0_604
